# baseline (speedup 1.0000x reference)
.LBB1_8:
	s_or_b64 exec, exec, s[4:5]
	s_waitcnt vmcnt(1)
	v_mov_b32_e32 v184, 1
	v_lshl_add_u32 v180, v176, 2, v172
	v_lshl_add_u32 v181, v177, 2, v172
	v_lshl_add_u32 v182, v178, 2, v172
	v_lshl_add_u32 v183, v179, 2, v172
	s_waitcnt lgkmcnt(0)
	ds_add_u32 v180, v184
	ds_add_u32 v181, v184
	ds_add_u32 v182, v184
	ds_add_u32 v183, v184
	s_waitcnt lgkmcnt(0)
	ds_read_b32 v151, v173
	s_waitcnt lgkmcnt(0)
	v_cvt_f32_i32_e32 v185, v151
	ds_write_b32 v173, v185 offset:256
	v_add_u32_e32 v10, v172, v2
	s_waitcnt vmcnt(1) lgkmcnt(0)
	s_barrier
	s_nop 0
	s_nop 0
	s_nop 0
	ds_read_b128 v[18:21], v10 offset:256
	ds_read_b128 v[22:25], v10 offset:288
	ds_read_b128 v[82:85], v10 offset:320
	ds_read_b128 v[86:89], v10 offset:352
	ds_read_b128 v[74:77], v10 offset:384
	ds_read_b128 v[78:81], v10 offset:416
	ds_read_b128 v[2:5], v213 offset:32768
	ds_read_b128 v[6:9], v213 offset:0
	ds_read_b128 v[66:69], v10 offset:448
	ds_read_b128 v[70:73], v10 offset:480
	ds_read_b128 v[10:13], v213 offset:1024
	s_waitcnt lgkmcnt(3)
	v_pk_mul_f32 v[26:27], v[8:9], v[20:21]
	v_pk_mul_f32 v[28:29], v[6:7], v[18:19]
	ds_read_b128 v[14:17], v213 offset:8192
	s_waitcnt lgkmcnt(1)
	v_pk_mul_f32 v[12:13], v[12:13], v[24:25]
	v_pk_mul_f32 v[10:11], v[10:11], v[22:23]
	v_pk_fma_f32 v[30:31], v[8:9], v[20:21], v[12:13]
	v_pk_fma_f32 v[32:33], v[6:7], v[18:19], v[10:11]
	v_cvt_pk_bf16_f32 v9, v12, v13
	v_cvt_pk_bf16_f32 v7, v26, v27
	v_cvt_pk_bf16_f32 v8, v10, v11
	v_cvt_pk_bf16_f32 v6, v28, v29
	ds_read_b128 v[10:13], v213 offset:33792
	s_nop 0
	v_mfma_f32_32x32x16_bf16 v[34:49], v[2:5], v[6:9], 0
	ds_read_b128 v[6:9], v213 offset:9216
	s_waitcnt lgkmcnt(2)
	v_mul_f32_e32 v26, v16, v20
	v_mul_f32_e32 v27, v17, v21
	v_pk_mul_f32 v[50:51], v[14:15], v[18:19]
	s_mov_b32 s4, 0x3727c5ac
	s_waitcnt lgkmcnt(0)
	v_pk_mul_f32 v[8:9], v[8:9], v[24:25]
	v_pk_mul_f32 v[28:29], v[6:7], v[22:23]
	v_pk_fma_f32 v[90:91], v[16:17], v[20:21], v[8:9]
	v_pk_fma_f32 v[92:93], v[14:15], v[18:19], v[28:29]
	ds_read_b128 v[14:17], v213 offset:2048
	v_cvt_pk_bf16_f32 v9, v8, v9
	v_cvt_pk_bf16_f32 v7, v26, v27
	v_cvt_pk_bf16_f32 v8, v28, v29
	ds_read_b128 v[26:29], v213 offset:3072
	v_cvt_pk_bf16_f32 v6, v50, v51
	s_waitcnt lgkmcnt(1)
	v_pk_mul_f32 v[94:95], v[14:15], v[82:83]
	s_mov_b32 s0, 0x3c800000
	v_mfma_f32_32x32x16_bf16 v[50:65], v[2:5], v[6:9], 0
	v_mul_f32_e32 v2, v16, v84
	v_mul_f32_e32 v3, v17, v85
	s_waitcnt lgkmcnt(0)
	v_mul_f32_e32 v4, v28, v88
	v_mul_f32_e32 v5, v29, v89
	v_pk_mul_f32 v[6:7], v[26:27], v[86:87]
	v_pk_fma_f32 v[8:9], v[16:17], v[84:85], v[4:5]
	v_cvt_pk_bf16_f32 v3, v2, v3
	v_pk_fma_f32 v[14:15], v[14:15], v[82:83], v[6:7]
	v_pk_add_f32 v[26:27], v[8:9], v[30:31]
	v_cvt_pk_bf16_f32 v5, v4, v5
	v_cvt_pk_bf16_f32 v4, v6, v7
	ds_read_b128 v[6:9], v213 offset:10240
	v_pk_add_f32 v[28:29], v[14:15], v[32:33]
	ds_read_b128 v[14:17], v213 offset:11264
	v_cvt_pk_bf16_f32 v2, v94, v95
	s_waitcnt lgkmcnt(1)
	v_pk_mul_f32 v[30:31], v[6:7], v[82:83]
	v_mov_b64_e32 v[152:153], s[4:5]
	v_mfma_f32_32x32x16_bf16 v[34:49], v[10:13], v[2:5], v[34:49]
	v_mul_f32_e32 v2, v8, v84
	v_mul_f32_e32 v3, v9, v85
	s_waitcnt lgkmcnt(0)
	v_mul_f32_e32 v4, v16, v88
	v_mul_f32_e32 v5, v17, v89
	v_pk_mul_f32 v[14:15], v[14:15], v[86:87]
	v_pk_fma_f32 v[8:9], v[8:9], v[84:85], v[4:5]
	v_pk_fma_f32 v[6:7], v[6:7], v[82:83], v[14:15]
	v_cvt_pk_bf16_f32 v5, v4, v5
	v_cvt_pk_bf16_f32 v3, v2, v3
	v_cvt_pk_bf16_f32 v4, v14, v15
	v_pk_add_f32 v[32:33], v[8:9], v[90:91]
	v_pk_add_f32 v[90:91], v[6:7], v[92:93]
	ds_read_b128 v[6:9], v213 offset:34816
	ds_read_b128 v[14:17], v213 offset:4096
	v_cvt_pk_bf16_f32 v2, v30, v31
	s_mov_b32 s13, 0
	s_mov_b64 s[6:7], 0
	v_mfma_f32_32x32x16_bf16 v[50:65], v[10:13], v[2:5], v[50:65]
	ds_read_b128 v[2:5], v213 offset:5120
	ds_read_b128 v[10:13], v213 offset:12288
	s_waitcnt lgkmcnt(2)
	v_pk_mul_f32 v[30:31], v[16:17], v[76:77]
	v_pk_mul_f32 v[92:93], v[14:15], v[74:75]
	s_waitcnt lgkmcnt(1)
	v_pk_mul_f32 v[4:5], v[4:5], v[80:81]
	v_pk_mul_f32 v[94:95], v[2:3], v[78:79]
	v_pk_fma_f32 v[2:3], v[16:17], v[76:77], v[4:5]
	v_cvt_pk_bf16_f32 v5, v4, v5
	v_pk_add_f32 v[96:97], v[2:3], v[26:27]
	v_cvt_pk_bf16_f32 v3, v30, v31
	v_cvt_pk_bf16_f32 v4, v94, v95
	v_cvt_pk_bf16_f32 v2, v92, v93
	v_pk_fma_f32 v[14:15], v[14:15], v[74:75], v[94:95]
	s_waitcnt lgkmcnt(0)
	v_pk_mul_f32 v[30:31], v[10:11], v[74:75]
	v_mfma_f32_32x32x16_bf16 v[34:49], v[6:9], v[2:5], v[34:49]
	ds_read_b128 v[2:5], v213 offset:13312
	v_add_f32_e32 v98, v14, v28
	v_add_f32_e32 v99, v15, v29
	ds_read_b128 v[14:17], v213 offset:35840
	v_pk_mul_f32 v[26:27], v[12:13], v[76:77]
	s_waitcnt lgkmcnt(1)
	v_pk_mul_f32 v[4:5], v[4:5], v[80:81]
	v_pk_mul_f32 v[28:29], v[2:3], v[78:79]
	v_pk_fma_f32 v[2:3], v[12:13], v[76:77], v[4:5]
	v_pk_fma_f32 v[10:11], v[10:11], v[74:75], v[28:29]
	v_pk_add_f32 v[32:33], v[2:3], v[32:33]
	v_pk_add_f32 v[92:93], v[10:11], v[90:91]
	ds_read_b128 v[10:13], v213 offset:6144
	v_cvt_pk_bf16_f32 v5, v4, v5
	v_cvt_pk_bf16_f32 v3, v26, v27
	v_cvt_pk_bf16_f32 v4, v28, v29
	ds_read_b128 v[26:29], v213 offset:7168
	v_cvt_pk_bf16_f32 v2, v30, v31
	s_waitcnt lgkmcnt(1)
	v_pk_mul_f32 v[30:31], v[10:11], v[66:67]
	v_mfma_f32_32x32x16_bf16 v[50:65], v[6:9], v[2:5], v[50:65]
	v_mul_f32_e32 v2, v12, v68
	v_mul_f32_e32 v3, v13, v69
	s_waitcnt lgkmcnt(0)
	v_mul_f32_e32 v4, v28, v72
	v_mul_f32_e32 v5, v29, v73
	v_pk_mul_f32 v[6:7], v[26:27], v[70:71]
	v_pk_fma_f32 v[8:9], v[12:13], v[68:69], v[4:5]
	v_cvt_pk_bf16_f32 v3, v2, v3
	v_pk_fma_f32 v[10:11], v[10:11], v[66:67], v[6:7]
	v_pk_add_f32 v[94:95], v[8:9], v[96:97]
	v_cvt_pk_bf16_f32 v5, v4, v5
	v_cvt_pk_bf16_f32 v4, v6, v7
	ds_read_b128 v[6:9], v213 offset:14336
	v_pk_add_f32 v[96:97], v[10:11], v[98:99]
	ds_read_b128 v[10:13], v213 offset:15360
	v_cvt_pk_bf16_f32 v2, v30, v31
	s_waitcnt lgkmcnt(1)
	v_pk_mul_f32 v[30:31], v[6:7], v[66:67]
	v_mfma_f32_32x32x16_bf16 v[34:49], v[14:17], v[2:5], v[34:49]
	s_waitcnt lgkmcnt(0)
	v_mul_f32_e32 v10, v10, v70
	v_mul_f32_e32 v11, v11, v71
	v_mul_f32_e32 v2, v8, v68
	v_mul_f32_e32 v3, v9, v69
	v_pk_mul_f32 v[4:5], v[12:13], v[72:73]
	v_pk_fma_f32 v[6:7], v[6:7], v[66:67], v[10:11]
	v_pk_fma_f32 v[8:9], v[8:9], v[68:69], v[4:5]
	v_pk_add_f32 v[92:93], v[6:7], v[92:93]
	v_cvt_pk_bf16_f32 v3, v2, v3
	v_pk_add_f32 v[90:91], v[8:9], v[32:33]
	v_cvt_pk_bf16_f32 v5, v4, v5
	v_cvt_pk_bf16_f32 v4, v10, v11
	ds_read_b128 v[26:29], v213 offset:36864
	ds_read_b128 v[6:9], v213 offset:16384
	v_cvt_pk_bf16_f32 v2, v30, v31
	ds_read_b128 v[98:101], v213 offset:25600
	ds_read_b128 v[102:105], v213 offset:37888
	v_mfma_f32_32x32x16_bf16 v[50:65], v[14:17], v[2:5], v[50:65]
	ds_read_b128 v[2:5], v213 offset:17408
	ds_read_b128 v[30:33], v213 offset:24576
	s_waitcnt lgkmcnt(4)
	v_pk_mul_f32 v[12:13], v[6:7], v[18:19]
	v_pk_mul_f32 v[10:11], v[8:9], v[20:21]
	s_waitcnt lgkmcnt(1)
	v_pk_mul_f32 v[14:15], v[2:3], v[22:23]
	v_pk_mul_f32 v[22:23], v[98:99], v[22:23]
	v_pk_fma_f32 v[112:113], v[6:7], v[18:19], v[14:15]
	s_waitcnt lgkmcnt(0)
	v_pk_mul_f32 v[114:115], v[30:31], v[18:19]
	v_pk_fma_f32 v[118:119], v[30:31], v[18:19], v[22:23]
	v_pk_mul_f32 v[4:5], v[4:5], v[24:25]
	v_pk_mul_f32 v[106:107], v[32:33], v[20:21]
	v_pk_mul_f32 v[24:25], v[100:101], v[24:25]
	ds_read_b128 v[98:101], v213 offset:18432
	v_cvt_pk_bf16_f32 v19, v106, v107
	ds_read_b128 v[106:109], v213 offset:19456
	v_pk_fma_f32 v[110:111], v[8:9], v[20:21], v[4:5]
	v_cvt_pk_bf16_f32 v5, v4, v5
	v_cvt_pk_bf16_f32 v3, v10, v11
	v_cvt_pk_bf16_f32 v4, v14, v15
	s_waitcnt lgkmcnt(0)
	v_pk_mul_f32 v[106:107], v[106:107], v[86:87]
	v_cvt_pk_bf16_f32 v2, v12, v13
	v_pk_mul_f32 v[120:121], v[98:99], v[82:83]
	v_pk_mul_f32 v[108:109], v[108:109], v[88:89]
	v_pk_fma_f32 v[98:99], v[98:99], v[82:83], v[106:107]
	v_mfma_f32_32x32x16_bf16 v[2:17], v[26:29], v[2:5], 0
	v_cvt_pk_bf16_f32 v18, v114, v115
	v_mul_f32_e32 v114, v100, v84
	v_mul_f32_e32 v115, v101, v85
	v_fma_f32 v100, v100, v84, v108
	v_fma_f32 v101, v101, v85, v109
	v_pk_add_f32 v[124:125], v[98:99], v[112:113]
	v_pk_add_f32 v[122:123], v[100:101], v[110:111]
	v_cvt_pk_bf16_f32 v101, v108, v109
	v_cvt_pk_bf16_f32 v100, v106, v107
	ds_read_b128 v[106:109], v213 offset:26624
	v_pk_fma_f32 v[116:117], v[32:33], v[20:21], v[24:25]
	v_cvt_pk_bf16_f32 v21, v24, v25
	v_cvt_pk_bf16_f32 v20, v22, v23
	ds_read_b128 v[110:113], v213 offset:27648
	v_cvt_pk_bf16_f32 v99, v114, v115
	v_mfma_f32_32x32x16_bf16 v[18:33], v[26:29], v[18:21], 0
	v_cvt_pk_bf16_f32 v98, v120, v121
	s_waitcnt lgkmcnt(1)
	v_mul_f32_e32 v114, v106, v82
	v_mul_f32_e32 v115, v107, v83
	s_waitcnt lgkmcnt(0)
	v_pk_mul_f32 v[86:87], v[110:111], v[86:87]
	v_pk_mul_f32 v[88:89], v[112:113], v[88:89]
	v_pk_fma_f32 v[82:83], v[106:107], v[82:83], v[86:87]
	v_mfma_f32_32x32x16_bf16 v[2:17], v[102:105], v[98:101], v[2:17]
	v_mul_f32_e32 v98, v108, v84
	v_mul_f32_e32 v99, v109, v85
	v_fma_f32 v84, v108, v84, v88
	v_fma_f32 v85, v109, v85, v89
	v_add_f32_e32 v108, v82, v118
	v_add_f32_e32 v109, v83, v119
	v_cvt_pk_bf16_f32 v83, v98, v99
	v_pk_add_f32 v[106:107], v[84:85], v[116:117]
	v_cvt_pk_bf16_f32 v85, v88, v89
	v_cvt_pk_bf16_f32 v84, v86, v87
	ds_read_b128 v[86:89], v213 offset:38912
	ds_read_b128 v[98:101], v213 offset:20480
	v_cvt_pk_bf16_f32 v82, v114, v115
	s_waitcnt lgkmcnt(0)
	v_pk_mul_f32 v[110:111], v[100:101], v[76:77]
	v_mfma_f32_32x32x16_bf16 v[18:33], v[102:105], v[82:85], v[18:33]
	ds_read_b128 v[82:85], v213 offset:21504
	ds_read_b128 v[102:105], v213 offset:28672
	v_mul_f32_e32 v112, v98, v74
	v_mul_f32_e32 v113, v99, v75
	s_waitcnt lgkmcnt(1)
	v_pk_mul_f32 v[84:85], v[84:85], v[80:81]
	v_pk_mul_f32 v[114:115], v[82:83], v[78:79]
	v_pk_fma_f32 v[82:83], v[100:101], v[76:77], v[84:85]
	v_cvt_pk_bf16_f32 v85, v84, v85
	v_pk_add_f32 v[116:117], v[82:83], v[122:123]
	v_cvt_pk_bf16_f32 v83, v110, v111
	v_cvt_pk_bf16_f32 v84, v114, v115
	v_cvt_pk_bf16_f32 v82, v112, v113
	v_pk_fma_f32 v[98:99], v[98:99], v[74:75], v[114:115]
	s_waitcnt lgkmcnt(0)
	v_pk_mul_f32 v[112:113], v[102:103], v[74:75]
	v_mfma_f32_32x32x16_bf16 v[2:17], v[86:89], v[82:85], v[2:17]
	ds_read_b128 v[82:85], v213 offset:29696
	v_add_f32_e32 v118, v98, v124
	v_add_f32_e32 v119, v99, v125
	v_mul_f32_e32 v110, v104, v76
	v_mul_f32_e32 v111, v105, v77
	ds_read_b128 v[98:101], v213 offset:39936
	s_waitcnt lgkmcnt(1)
	v_pk_mul_f32 v[78:79], v[82:83], v[78:79]
	v_pk_mul_f32 v[80:81], v[84:85], v[80:81]
	v_pk_fma_f32 v[74:75], v[102:103], v[74:75], v[78:79]
	v_pk_fma_f32 v[76:77], v[104:105], v[76:77], v[80:81]
	v_pk_add_f32 v[104:105], v[74:75], v[108:109]
	v_pk_add_f32 v[102:103], v[76:77], v[106:107]
	v_cvt_pk_bf16_f32 v77, v80, v81
	v_cvt_pk_bf16_f32 v76, v78, v79
	ds_read_b128 v[78:81], v213 offset:22528
	ds_read_b128 v[82:85], v213 offset:23552
	v_cvt_pk_bf16_f32 v75, v110, v111
	v_cvt_pk_bf16_f32 v74, v112, v113
	s_waitcnt lgkmcnt(0)
	v_pk_mul_f32 v[82:83], v[82:83], v[70:71]
	v_mfma_f32_32x32x16_bf16 v[18:33], v[86:89], v[74:77], v[18:33]
	v_mul_f32_e32 v74, v80, v68
	v_mul_f32_e32 v75, v81, v69
	v_mul_f32_e32 v76, v84, v72
	v_mul_f32_e32 v77, v85, v73
	v_mul_f32_e32 v86, v78, v66
	v_mul_f32_e32 v87, v79, v67
	v_pk_fma_f32 v[80:81], v[80:81], v[68:69], v[76:77]
	v_pk_fma_f32 v[78:79], v[78:79], v[66:67], v[82:83]
	v_cvt_pk_bf16_f32 v75, v74, v75
	v_pk_add_f32 v[88:89], v[80:81], v[116:117]
	v_pk_add_f32 v[106:107], v[78:79], v[118:119]
	ds_read_b128 v[78:81], v213 offset:30720
	v_cvt_pk_bf16_f32 v77, v76, v77
	v_cvt_pk_bf16_f32 v76, v82, v83
	ds_read_b128 v[82:85], v213 offset:31744
	v_cvt_pk_bf16_f32 v74, v86, v87
	s_waitcnt lgkmcnt(0)
	v_pk_mul_f32 v[72:73], v[84:85], v[72:73]
	v_mfma_f32_32x32x16_bf16 v[2:17], v[98:101], v[74:77], v[2:17]
	v_mul_f32_e32 v74, v80, v68
	v_mul_f32_e32 v75, v81, v69
	v_fma_f32 v68, v80, v68, v72
	v_fma_f32 v69, v81, v69, v73
	v_mul_f32_e32 v70, v82, v70
	v_mul_f32_e32 v71, v83, v71
	v_pk_add_f32 v[84:85], v[68:69], v[102:103]
	v_cvt_pk_bf16_f32 v69, v72, v73
	v_add_f32_e32 v72, v97, v96
	v_add_f32_e32 v73, v94, v95
	v_pk_mul_f32 v[76:77], v[78:79], v[66:67]
	v_pk_fma_f32 v[66:67], v[78:79], v[66:67], v[70:71]
	v_add_f32_e32 v72, v72, v73
	v_pk_add_f32 v[86:87], v[66:67], v[104:105]
	v_mov_b32_e32 v66, v72
	s_nop 1
	v_permlane32_swap_b32_e32 v72, v66
	v_add_f32_e32 v66, v72, v66
	v_cvt_pk_bf16_f32 v67, v74, v75
	v_rcp_f32_e32 v74, v66
	v_cvt_pk_bf16_f32 v68, v70, v71
	v_cvt_pk_bf16_f32 v66, v76, v77
	v_pk_mul_f32 v[70:71], v[46:47], v[74:75] op_sel_hi:[1,0]
	s_nop 0
	v_mfma_f32_32x32x16_bf16 v[18:33], v[98:101], v[66:69], v[18:33]
	v_mul_f32_e32 v66, v42, v74
	v_mul_f32_e32 v67, v43, v74
	v_add_f32_e32 v42, v93, v92
	v_add_f32_e32 v43, v90, v91
	v_pk_mul_f32 v[68:69], v[44:45], v[74:75] op_sel_hi:[1,0]
	v_add_f32_e32 v42, v42, v43
	v_mov_b32_e32 v43, v42
	s_nop 1
	v_permlane32_swap_b32_e32 v42, v43
	v_add_f32_e32 v42, v42, v43
	v_rcp_f32_e32 v42, v42
	v_add_f32_e32 v44, v107, v106
	v_add_f32_e32 v45, v88, v89
	v_pk_mul_f32 v[72:73], v[48:49], v[74:75] op_sel_hi:[1,0]
	v_add_f32_e32 v44, v44, v45
	v_pk_mul_f32 v[36:37], v[36:37], v[74:75] op_sel_hi:[1,0]
	v_pk_mul_f32 v[38:39], v[38:39], v[74:75] op_sel_hi:[1,0]
	v_pk_mul_f32 v[40:41], v[40:41], v[74:75] op_sel_hi:[1,0]
	v_pk_mul_f32 v[34:35], v[34:35], v[74:75] op_sel_hi:[1,0]
	v_pk_mul_f32 v[74:75], v[58:59], v[42:43] op_sel_hi:[1,0]
	v_pk_mul_f32 v[78:79], v[60:61], v[42:43] op_sel_hi:[1,0]
	v_pk_mul_f32 v[80:81], v[62:63], v[42:43] op_sel_hi:[1,0]
	v_pk_mul_f32 v[82:83], v[64:65], v[42:43] op_sel_hi:[1,0]
	v_pk_mul_f32 v[92:93], v[52:53], v[42:43] op_sel_hi:[1,0]
	v_mov_b32_e32 v43, v44
	s_nop 1
	v_permlane32_swap_b32_e32 v44, v43
	v_add_f32_e32 v43, v44, v43
	v_rcp_f32_e32 v76, v43
	v_pk_mul_f32 v[96:97], v[54:55], v[42:43] op_sel_hi:[1,0]
	v_pk_mul_f32 v[94:95], v[56:57], v[42:43] op_sel_hi:[1,0]
	v_pk_mul_f32 v[98:99], v[50:51], v[42:43] op_sel_hi:[1,0]
	v_pk_mul_f32 v[100:101], v[4:5], v[76:77] op_sel_hi:[1,0]
	v_pk_mov_b32 v[4:5], v[86:87], v[84:85] op_sel:[1,0]
	v_mov_b32_e32 v87, v85
	v_pk_add_f32 v[4:5], v[4:5], v[86:87]
	v_pk_mul_f32 v[102:103], v[6:7], v[76:77] op_sel_hi:[1,0]
	v_pk_add_f32 v[104:105], v[4:5], v[4:5] op_sel:[0,1] op_sel_hi:[1,0]
	v_cvt_pk_bf16_f32 v7, v40, v41
	ds_read_b128 v[84:87], v150 offset:52224
	ds_read_b128 v[50:53], v150 offset:35840
	ds_read_b128 v[54:57], v150 offset:36864
	ds_read_b128 v[58:61], v150 offset:37888
	ds_read_b128 v[62:65], v150 offset:38912
	v_cvt_pk_bf16_f32 v6, v38, v39
	v_cvt_pk_bf16_f32 v5, v36, v37
	v_cvt_pk_bf16_f32 v4, v34, v35
	ds_read_b128 v[88:91], v150 offset:53248
	ds_read_b128 v[34:37], v150 offset:39936
	ds_read_b128 v[38:41], v150 offset:40960
	ds_read_b128 v[42:45], v150 offset:41984
	ds_read_b128 v[46:49], v150 offset:43008
	v_cvt_pk_bf16_f32 v95, v94, v95
	v_cvt_pk_bf16_f32 v94, v96, v97
	v_cvt_pk_bf16_f32 v93, v92, v93
	v_cvt_pk_bf16_f32 v92, v98, v99
	s_waitcnt lgkmcnt(5)
	v_mfma_f32_32x32x16_bf16 v[50:65], v[84:87], v[4:7], v[50:65]
	v_mul_f32_e32 v10, v10, v76
	v_mul_f32_e32 v11, v11, v76
	v_mul_f32_e32 v12, v12, v76
	v_mul_f32_e32 v13, v13, v76
	v_mul_f32_e32 v8, v8, v76
	v_mul_f32_e32 v9, v9, v76
	v_mov_b32_e32 v77, v104
	s_nop 1
	v_permlane32_swap_b32_e32 v104, v77
	v_cvt_pk_bf16_f32 v73, v72, v73
	s_waitcnt lgkmcnt(0)
	v_mfma_f32_32x32x16_bf16 v[34:49], v[84:87], v[92:95], v[34:49]
	v_cvt_pk_bf16_f32 v72, v70, v71
	v_cvt_pk_bf16_f32 v70, v66, v67
	v_add_f32_e32 v66, v104, v77
	v_cvt_pk_bf16_f32 v71, v68, v69
	v_rcp_f32_e32 v104, v66
	v_cvt_pk_bf16_f32 v69, v82, v83
	v_cvt_pk_bf16_f32 v68, v80, v81
	v_cvt_pk_bf16_f32 v67, v78, v79
	v_cvt_pk_bf16_f32 v66, v74, v75
	ds_read_b128 v[78:81], v150 offset:54272
	v_mfma_f32_32x32x16_bf16 v[50:65], v[88:91], v[70:73], v[50:65]
	v_mul_f32_e32 v2, v2, v76
	v_mul_f32_e32 v3, v3, v76
	v_mul_f32_e32 v20, v20, v104
	v_mul_f32_e32 v21, v21, v104
	v_cvt_pk_bf16_f32 v85, v8, v9
	v_cvt_pk_bf16_f32 v82, v2, v3
	v_pk_mul_f32 v[2:3], v[22:23], v[104:105] op_sel_hi:[1,0]
	v_pk_mul_f32 v[8:9], v[24:25], v[104:105] op_sel_hi:[1,0]
	v_pk_mul_f32 v[18:19], v[18:19], v[104:105] op_sel_hi:[1,0]
	v_mfma_f32_32x32x16_bf16 v[34:49], v[88:91], v[66:69], v[34:49]
	v_cvt_pk_bf16_f32 v84, v102, v103
	v_cvt_pk_bf16_f32 v83, v100, v101
	ds_read_b128 v[86:89], v150 offset:55296
	v_cvt_pk_bf16_f32 v99, v8, v9
	v_cvt_pk_bf16_f32 v98, v2, v3
	v_cvt_pk_bf16_f32 v97, v20, v21
	v_cvt_pk_bf16_f32 v96, v18, v19
	s_waitcnt lgkmcnt(1)
	v_mfma_f32_32x32x16_bf16 v[50:65], v[78:81], v[82:85], v[50:65]
	v_mul_f32_e32 v2, v14, v76
	v_mul_f32_e32 v3, v15, v76
	v_mul_f32_e32 v8, v16, v76
	v_mul_f32_e32 v9, v17, v76
	v_mul_f32_e32 v14, v26, v104
	v_mul_f32_e32 v15, v27, v104
	v_cvt_pk_bf16_f32 v77, v8, v9
	v_cvt_pk_bf16_f32 v76, v2, v3
	v_cvt_pk_bf16_f32 v74, v10, v11
	v_pk_mul_f32 v[2:3], v[28:29], v[104:105] op_sel_hi:[1,0]
	v_mfma_f32_32x32x16_bf16 v[34:49], v[78:81], v[96:99], v[34:49]
	v_mul_f32_e32 v8, v30, v104
	v_mul_f32_e32 v9, v31, v104
	v_mul_f32_e32 v10, v32, v104
	v_mul_f32_e32 v11, v33, v104
	v_cvt_pk_bf16_f32 v75, v12, v13
	v_cvt_pk_bf16_f32 v81, v10, v11
	v_cvt_pk_bf16_f32 v80, v8, v9
	v_cvt_pk_bf16_f32 v79, v2, v3
	v_cvt_pk_bf16_f32 v78, v14, v15
	s_waitcnt lgkmcnt(0)
	v_mfma_f32_32x32x16_bf16 v[50:65], v[86:89], v[74:77], v[50:65]
	v_mfma_f32_32x32x16_bf16 v[34:49], v[86:89], v[78:81], v[34:49]
	ds_read_b128 v[86:89], v150 offset:56320
	ds_read_b128 v[18:21], v150 offset:44032
	ds_read_b128 v[22:25], v150 offset:45056
	ds_read_b128 v[26:29], v150 offset:46080
	ds_read_b128 v[30:33], v150 offset:47104
	ds_read_b128 v[100:103], v150 offset:57344
	s_waitcnt lgkmcnt(1)
	v_mfma_f32_32x32x16_bf16 v[18:33], v[86:89], v[4:7], v[18:33]
	ds_read_b128 v[2:5], v150 offset:48128
	ds_read_b128 v[6:9], v150 offset:49152
	ds_read_b128 v[10:13], v150 offset:50176
	ds_read_b128 v[14:17], v150 offset:51200
	s_waitcnt lgkmcnt(0)
	v_mfma_f32_32x32x16_bf16 v[2:17], v[86:89], v[92:95], v[2:17]
	v_mfma_f32_32x32x16_bf16 v[18:33], v[100:103], v[70:73], v[18:33]
	v_mfma_f32_32x32x16_bf16 v[2:17], v[100:103], v[66:69], v[2:17]
	ds_read_b128 v[66:69], v150 offset:58368
	ds_read_b128 v[70:73], v150 offset:59392
	s_waitcnt lgkmcnt(1)
	v_mfma_f32_32x32x16_bf16 v[18:33], v[66:69], v[82:85], v[18:33]
	v_mfma_f32_32x32x16_bf16 v[2:17], v[66:69], v[96:99], v[2:17]
	s_waitcnt lgkmcnt(0)
	v_mfma_f32_32x32x16_bf16 v[18:33], v[70:73], v[74:77], v[18:33]
	v_mfma_f32_32x32x16_bf16 v[2:17], v[70:73], v[78:81], v[2:17]
	s_nop 10
	v_mul_f32_e32 v66, v22, v22
	v_mul_f32_e32 v67, v23, v23
	v_mul_f32_e32 v68, v30, v30
	v_mul_f32_e32 v69, v31, v31
	v_mul_f32_e32 v70, v24, v24
	v_mul_f32_e32 v71, v25, v25
	v_pk_mul_f32 v[72:73], v[32:33], v[32:33]
	v_pk_mul_f32 v[74:75], v[20:21], v[20:21]
	v_pk_mul_f32 v[76:77], v[28:29], v[28:29]
	v_pk_mul_f32 v[78:79], v[26:27], v[26:27]
	v_pk_mul_f32 v[80:81], v[18:19], v[18:19]
	v_pk_fma_f32 v[78:79], v[58:59], v[58:59], v[78:79]
	v_pk_fma_f32 v[76:77], v[60:61], v[60:61], v[76:77]
	v_pk_fma_f32 v[74:75], v[52:53], v[52:53], v[74:75]
	v_pk_fma_f32 v[72:73], v[64:65], v[64:65], v[72:73]
	v_pk_fma_f32 v[70:71], v[56:57], v[56:57], v[70:71]
	v_pk_fma_f32 v[68:69], v[62:63], v[62:63], v[68:69]
	v_pk_fma_f32 v[66:67], v[54:55], v[54:55], v[66:67]
	v_pk_fma_f32 v[80:81], v[50:51], v[50:51], v[80:81]
	v_pk_add_f32 v[66:67], v[66:67], v[68:69]
	v_pk_add_f32 v[68:69], v[70:71], v[72:73]
	v_pk_add_f32 v[70:71], v[74:75], v[76:77]
	v_pk_add_f32 v[72:73], v[80:81], v[78:79]
	v_pk_add_f32 v[68:69], v[70:71], v[68:69]
	v_pk_add_f32 v[66:67], v[72:73], v[66:67]
	v_pk_mul_f32 v[72:73], v[14:15], v[14:15]
	v_pk_mov_b32 v[70:71], v[66:67], v[68:69] op_sel:[1,0]
	v_mov_b32_e32 v67, v69
	v_pk_add_f32 v[66:67], v[70:71], v[66:67]
	v_pk_mul_f32 v[70:71], v[6:7], v[6:7]
	v_pk_mul_f32 v[74:75], v[8:9], v[8:9]
	v_pk_mul_f32 v[76:77], v[16:17], v[16:17]
	v_pk_mul_f32 v[78:79], v[4:5], v[4:5]
	v_pk_mul_f32 v[80:81], v[12:13], v[12:13]
	v_pk_mul_f32 v[82:83], v[10:11], v[10:11]
	v_pk_mul_f32 v[84:85], v[2:3], v[2:3]
	v_pk_fma_f32 v[82:83], v[42:43], v[42:43], v[82:83]
	v_pk_fma_f32 v[80:81], v[44:45], v[44:45], v[80:81]
	v_pk_fma_f32 v[78:79], v[36:37], v[36:37], v[78:79]
	v_pk_fma_f32 v[76:77], v[48:49], v[48:49], v[76:77]
	v_pk_fma_f32 v[74:75], v[40:41], v[40:41], v[74:75]
	v_pk_fma_f32 v[72:73], v[46:47], v[46:47], v[72:73]
	v_pk_fma_f32 v[70:71], v[38:39], v[38:39], v[70:71]
	v_pk_fma_f32 v[84:85], v[34:35], v[34:35], v[84:85]
	v_pk_add_f32 v[70:71], v[70:71], v[72:73]
	v_pk_add_f32 v[72:73], v[74:75], v[76:77]
	v_pk_add_f32 v[74:75], v[78:79], v[80:81]
	v_pk_add_f32 v[76:77], v[84:85], v[82:83]
	v_pk_add_f32 v[72:73], v[74:75], v[72:73]
	v_pk_add_f32 v[70:71], v[76:77], v[70:71]
	v_pk_add_f32 v[66:67], v[66:67], v[66:67] op_sel:[0,1] op_sel_hi:[1,0]
	v_add_f32_e32 v70, v71, v70
	v_add_f32_e32 v71, v72, v73
	v_mov_b32_e32 v69, v66
	v_add_f32_e32 v70, v70, v71
	s_nop 0
	v_permlane32_swap_b32_e32 v66, v69
	v_mov_b32_e32 v68, v70
	s_nop 1
	v_permlane32_swap_b32_e32 v70, v68
	v_mov_b32_e32 v71, v66
	v_pk_add_f32 v[66:67], v[70:71], v[68:69]
	v_pk_fma_f32 v[66:67], v[66:67], s[0:1], v[152:153] op_sel_hi:[1,0,0]
	s_mov_b32 s1, 0x800000
	v_rsq_f32_e32 v68, v67
	s_nop 0
	v_pk_mul_f32 v[158:159], v[50:51], v[68:69] op_sel_hi:[1,0]
	v_pk_mul_f32 v[50:51], v[18:19], v[68:69] op_sel_hi:[1,0]
	v_pk_mul_f32 v[80:81], v[60:61], v[68:69] op_sel_hi:[1,0]
	v_pk_mul_f32 v[60:61], v[28:29], v[68:69] op_sel_hi:[1,0]
	v_pk_mul_f32 v[78:79], v[58:59], v[68:69] op_sel_hi:[1,0]
	v_pk_mul_f32 v[160:161], v[52:53], v[68:69] op_sel_hi:[1,0]
	v_pk_mul_f32 v[82:83], v[54:55], v[68:69] op_sel_hi:[1,0]
	v_rsq_f32_e32 v28, v66
	v_pk_mul_f32 v[168:169], v[56:57], v[68:69] op_sel_hi:[1,0]
	v_pk_mul_f32 v[58:59], v[26:27], v[68:69] op_sel_hi:[1,0]
	v_pk_mul_f32 v[52:53], v[20:21], v[68:69] op_sel_hi:[1,0]
	v_pk_mul_f32 v[54:55], v[22:23], v[68:69] op_sel_hi:[1,0]
	v_pk_mul_f32 v[56:57], v[24:25], v[68:69] op_sel_hi:[1,0]
	v_pk_mul_f32 v[18:19], v[42:43], v[28:29] op_sel_hi:[1,0]
	v_pk_mul_f32 v[20:21], v[44:45], v[28:29] op_sel_hi:[1,0]
	v_pk_mul_f32 v[22:23], v[46:47], v[28:29] op_sel_hi:[1,0]
	v_pk_mul_f32 v[26:27], v[48:49], v[28:29] op_sel_hi:[1,0]
	v_pk_mul_f32 v[162:163], v[34:35], v[28:29] op_sel_hi:[1,0]
	v_pk_mul_f32 v[164:165], v[36:37], v[28:29] op_sel_hi:[1,0]
	v_pk_mul_f32 v[166:167], v[38:39], v[28:29] op_sel_hi:[1,0]
	v_pk_mul_f32 v[24:25], v[40:41], v[28:29] op_sel_hi:[1,0]
	v_pk_mul_f32 v[104:105], v[2:3], v[28:29] op_sel_hi:[1,0]
	v_pk_mul_f32 v[112:113], v[4:5], v[28:29] op_sel_hi:[1,0]
	ds_read_b128 v[2:5], v150 offset:60416
	ds_read_b128 v[34:37], v174 offset:32768
	ds_read_b128 v[38:41], v174 offset:32800
	ds_read_b128 v[42:45], v174 offset:32832
	ds_read_b128 v[46:49], v174 offset:32864
	v_cvt_pk_bf16_f32 v129, v168, v169
	v_cvt_pk_bf16_f32 v128, v82, v83
	v_cvt_pk_bf16_f32 v127, v160, v161
	v_cvt_pk_bf16_f32 v126, v158, v159
	v_cvt_pk_bf16_f32 v137, v24, v25
	v_cvt_pk_bf16_f32 v136, v166, v167
	v_cvt_pk_bf16_f32 v135, v164, v165
	s_waitcnt lgkmcnt(0)
	v_mfma_f32_32x32x16_bf16 v[86:101], v[2:5], v[126:129], v[34:49]
	v_cvt_pk_bf16_f32 v134, v162, v163
	v_mul_f32_e32 v84, v62, v68
	v_mul_f32_e32 v85, v63, v68
	v_mul_f32_e32 v170, v64, v68
	v_mul_f32_e32 v171, v65, v68
	v_pk_mul_f32 v[62:63], v[30:31], v[68:69] op_sel_hi:[1,0]
	v_pk_mul_f32 v[64:65], v[32:33], v[68:69] op_sel_hi:[1,0]
	v_pk_mul_f32 v[116:117], v[6:7], v[28:29] op_sel_hi:[1,0]
	v_pk_mul_f32 v[154:155], v[8:9], v[28:29] op_sel_hi:[1,0]
	v_mfma_f32_32x32x16_bf16 v[34:49], v[2:5], v[134:137], v[34:49]
	ds_read_b128 v[6:9], v150 offset:61440
	ds_read_b128 v[66:69], v174 offset:32896
	ds_read_b128 v[106:109], v150 offset:64512
	v_cvt_pk_bf16_f32 v125, v170, v171
	v_cvt_pk_bf16_f32 v124, v84, v85
	v_cvt_pk_bf16_f32 v123, v80, v81
	v_cvt_pk_bf16_f32 v122, v78, v79
	v_cvt_pk_bf16_f32 v149, v26, v27
	v_cvt_pk_bf16_f32 v148, v22, v23
	v_cvt_pk_bf16_f32 v147, v20, v21
	v_cvt_pk_bf16_f32 v146, v18, v19
	s_waitcnt lgkmcnt(2)
	v_mfma_f32_32x32x16_bf16 v[86:101], v[6:9], v[122:125], v[86:101]
	v_mul_f32_e32 v102, v10, v28
	v_mul_f32_e32 v103, v11, v28
	v_mul_f32_e32 v110, v12, v28
	v_mul_f32_e32 v111, v13, v28
	v_mul_f32_e32 v114, v14, v28
	v_mul_f32_e32 v115, v15, v28
	v_pk_mul_f32 v[156:157], v[16:17], v[28:29] op_sel_hi:[1,0]
	ds_read_b128 v[176:179], v174 offset:33536
	ds_read_b128 v[180:183], v174 offset:33568
	ds_read_b128 v[184:187], v174 offset:33600
	ds_read_b128 v[28:31], v174 offset:33632
	ds_read_b128 v[188:191], v174 offset:33792
	ds_read_b128 v[192:195], v174 offset:33824
	ds_read_b128 v[196:199], v174 offset:33856
	ds_read_b128 v[200:203], v174 offset:33888
	ds_read_b128 v[204:207], v150 offset:62464
	v_cvt_pk_bf16_f32 v133, v56, v57
	v_mfma_f32_32x32x16_bf16 v[34:49], v[6:9], v[146:149], v[34:49]
	v_cvt_pk_bf16_f32 v132, v54, v55
	v_cvt_pk_bf16_f32 v131, v52, v53
	v_cvt_pk_bf16_f32 v130, v50, v51
	ds_read_b128 v[70:73], v174 offset:33664
	ds_read_b128 v[74:77], v174 offset:33920
	ds_read_b128 v[208:211], v150 offset:63488
	v_cvt_pk_bf16_f32 v145, v154, v155
	v_cvt_pk_bf16_f32 v144, v116, v117
	v_cvt_pk_bf16_f32 v143, v112, v113
	v_cvt_pk_bf16_f32 v142, v104, v105
	s_waitcnt lgkmcnt(3)
	v_mfma_f32_32x32x16_bf16 v[86:101], v[204:207], v[130:133], v[86:101]
	v_cvt_pk_bf16_f32 v121, v64, v65
	v_cvt_pk_bf16_f32 v120, v62, v63
	v_cvt_pk_bf16_f32 v119, v60, v61
	v_cvt_pk_bf16_f32 v118, v58, v59
	v_cvt_pk_bf16_f32 v141, v156, v157
	v_cvt_pk_bf16_f32 v140, v114, v115
	v_cvt_pk_bf16_f32 v139, v110, v111
	v_mfma_f32_32x32x16_bf16 v[34:49], v[204:207], v[142:145], v[34:49]
	v_cvt_pk_bf16_f32 v138, v102, v103
	v_fma_f32 v16, v30, v170, v202
	v_fma_f32 v17, v31, v171, v203
	v_fma_f32 v14, v28, v84, v200
	v_fma_f32 v15, v29, v85, v201
	v_pk_fma_f32 v[12:13], v[186:187], v[80:81], v[198:199]
	v_pk_fma_f32 v[10:11], v[184:185], v[78:79], v[196:197]
	v_pk_fma_f32 v[8:9], v[182:183], v[168:169], v[194:195]
	s_waitcnt lgkmcnt(0)
	v_mfma_f32_32x32x16_bf16 v[86:101], v[208:211], v[118:121], v[86:101]
	v_fma_f32 v6, v180, v82, v192
	v_fma_f32 v7, v181, v83, v193
	ds_read_b128 v[78:81], v174 offset:33760
	ds_read_b128 v[82:85], v174 offset:33248
	v_fma_f32 v4, v178, v160, v190
	v_fma_f32 v5, v179, v161, v191
	v_pk_fma_f32 v[2:3], v[176:177], v[158:159], v[188:189]
	v_pk_fma_f32 v[32:33], v[30:31], v[26:27], v[202:203]
	v_pk_fma_f32 v[30:31], v[28:29], v[22:23], v[200:201]
	v_pk_fma_f32 v[28:29], v[186:187], v[20:21], v[198:199]
	v_pk_fma_f32 v[26:27], v[184:185], v[18:19], v[196:197]
	v_pk_fma_f32 v[24:25], v[182:183], v[24:25], v[194:195]
	v_pk_fma_f32 v[22:23], v[180:181], v[166:167], v[192:193]
	v_pk_fma_f32 v[20:21], v[178:179], v[164:165], v[190:191]
	v_pk_fma_f32 v[18:19], v[176:177], v[162:163], v[188:189]
	ds_read_b128 v[158:161], v174 offset:33696
	ds_read_b128 v[162:165], v174 offset:33728
	ds_read_b128 v[166:169], v174 offset:33952
	ds_read_b128 v[176:179], v174 offset:33984
	ds_read_b128 v[180:183], v174 offset:34016
	ds_read_b128 v[184:187], v212 offset:11264
	v_mfma_f32_32x32x16_bf16 v[34:49], v[208:211], v[138:141], v[34:49]
	v_cvt_pk_bf16_f32 v86, v86, v87
	v_cvt_pk_bf16_f32 v87, v88, v89
	v_cvt_pk_bf16_f32 v88, v90, v91
	v_cvt_pk_bf16_f32 v89, v92, v93
	ds_read_b128 v[90:93], v212 offset:12288
	v_pk_max_i16 v86, v86, 0
	v_pk_max_i16 v87, v87, 0
	v_pk_max_i16 v88, v88, 0
	v_pk_max_i16 v89, v89, 0
	s_nop 1
	s_nop 0
	v_cvt_pk_bf16_f32 v188, v34, v35
	v_cvt_pk_bf16_f32 v189, v36, v37
	v_cvt_pk_bf16_f32 v190, v38, v39
	v_cvt_pk_bf16_f32 v191, v40, v41
	s_waitcnt lgkmcnt(1)
	v_mfma_f32_32x32x16_bf16 v[2:17], v[184:187], v[86:89], v[2:17]
	v_pk_max_i16 v188, v188, 0
	v_pk_max_i16 v189, v189, 0
	v_pk_max_i16 v190, v190, 0
	v_pk_max_i16 v191, v191, 0
	v_cvt_pk_bf16_f32 v94, v94, v95
	v_cvt_pk_bf16_f32 v95, v96, v97
	v_cvt_pk_bf16_f32 v96, v98, v99
	v_cvt_pk_bf16_f32 v97, v100, v101
	v_cvt_pk_bf16_f32 v98, v42, v43
	v_cvt_pk_bf16_f32 v99, v44, v45
	v_mfma_f32_32x32x16_bf16 v[18:33], v[184:187], v[188:191], v[18:33]
	ds_read_b128 v[184:187], v212 offset:19456
	v_cvt_pk_bf16_f32 v100, v46, v47
	v_cvt_pk_bf16_f32 v101, v48, v49
	v_fma_f32 v64, v80, v64, v182
	v_fma_f32 v65, v81, v65, v183
	v_pk_fma_f32 v[62:63], v[78:79], v[62:63], v[180:181]
	v_pk_fma_f32 v[60:61], v[164:165], v[60:61], v[178:179]
	v_pk_fma_f32 v[58:59], v[162:163], v[58:59], v[176:177]
	v_pk_max_i16 v94, v94, 0
	v_pk_max_i16 v95, v95, 0
	v_pk_max_i16 v96, v96, 0
	v_pk_max_i16 v97, v97, 0
	v_pk_max_i16 v98, v98, 0
	v_pk_max_i16 v99, v99, 0
	v_pk_max_i16 v100, v100, 0
	v_pk_max_i16 v101, v101, 0
	v_pk_fma_f32 v[56:57], v[160:161], v[56:57], v[168:169]
	s_waitcnt lgkmcnt(1)
	v_mfma_f32_32x32x16_bf16 v[2:17], v[90:93], v[94:97], v[2:17]
	v_fma_f32 v54, v158, v54, v166
	v_fma_f32 v55, v159, v55, v167
	v_fma_f32 v52, v72, v52, v76
	v_fma_f32 v53, v73, v53, v77
	v_fma_f32 v50, v70, v50, v74
	v_fma_f32 v51, v71, v51, v75
	v_pk_fma_f32 v[48:49], v[80:81], v[156:157], v[182:183]
	v_pk_fma_f32 v[46:47], v[78:79], v[114:115], v[180:181]
	v_pk_fma_f32 v[44:45], v[164:165], v[110:111], v[178:179]
	v_pk_fma_f32 v[42:43], v[162:163], v[102:103], v[176:177]
	v_mfma_f32_32x32x16_bf16 v[18:33], v[90:93], v[98:101], v[18:33]
	ds_read_b128 v[90:93], v212 offset:20480
	v_fma_f32 v40, v160, v154, v168
	v_fma_f32 v41, v161, v155, v169
	v_fma_f32 v38, v158, v116, v166
	v_fma_f32 v39, v159, v117, v167
	v_pk_fma_f32 v[36:37], v[72:73], v[112:113], v[76:77]
	v_pk_fma_f32 v[34:35], v[70:71], v[104:105], v[74:75]
	s_waitcnt lgkmcnt(1)
	v_mfma_f32_32x32x16_bf16 v[50:65], v[184:187], v[86:89], v[50:65]
	ds_read_b128 v[70:73], v174 offset:32928
	ds_read_b128 v[74:77], v174 offset:32960
	ds_read_b128 v[78:81], v174 offset:32992
	ds_read_b128 v[86:89], v174 offset:33024
	ds_read_b128 v[110:113], v212 offset:1024
	v_mfma_f32_32x32x16_bf16 v[34:49], v[184:187], v[188:191], v[34:49]
	s_waitcnt lgkmcnt(5)
	v_mfma_f32_32x32x16_bf16 v[50:65], v[90:93], v[94:97], v[50:65]
	v_mfma_f32_32x32x16_bf16 v[34:49], v[90:93], v[98:101], v[34:49]
	s_waitcnt lgkmcnt(2)
	v_mfma_f32_32x32x16_bf16 v[90:105], v[106:109], v[126:129], v[66:81]
	v_mfma_f32_32x32x16_bf16 v[66:81], v[106:109], v[134:137], v[66:81]
	ds_read_b128 v[106:109], v212 offset:0
	s_waitcnt lgkmcnt(0)
	v_mfma_f32_32x32x16_bf16 v[90:105], v[106:109], v[122:125], v[90:105]
	v_mfma_f32_32x32x16_bf16 v[66:81], v[106:109], v[146:149], v[66:81]
	ds_read_b128 v[106:109], v212 offset:2048
	v_mfma_f32_32x32x16_bf16 v[90:105], v[110:113], v[130:133], v[90:105]
	v_mfma_f32_32x32x16_bf16 v[66:81], v[110:113], v[142:145], v[66:81]
	ds_read_b128 v[110:113], v212 offset:13312
	s_waitcnt lgkmcnt(1)
	v_mfma_f32_32x32x16_bf16 v[90:105], v[106:109], v[118:121], v[90:105]
	v_mfma_f32_32x32x16_bf16 v[66:81], v[106:109], v[138:141], v[66:81]
	s_nop 10
	v_cvt_pk_bf16_f32 v90, v90, v91
	v_cvt_pk_bf16_f32 v91, v92, v93
	v_cvt_pk_bf16_f32 v92, v94, v95
	v_cvt_pk_bf16_f32 v94, v98, v99
	v_cvt_pk_bf16_f32 v95, v100, v101
	ds_read_b128 v[98:101], v212 offset:21504
	v_cvt_pk_bf16_f32 v66, v66, v67
	v_cvt_pk_bf16_f32 v67, v68, v69
	v_cvt_pk_bf16_f32 v68, v70, v71
	v_cvt_pk_bf16_f32 v93, v96, v97
	v_cvt_pk_bf16_f32 v69, v72, v73
	ds_read_b128 v[70:73], v212 offset:14336
	v_pk_max_i16 v90, v90, 0
	v_pk_max_i16 v91, v91, 0
	v_pk_max_i16 v92, v92, 0
	v_pk_max_i16 v93, v93, 0
	v_pk_max_i16 v66, v66, 0
	v_pk_max_i16 v67, v67, 0
	v_pk_max_i16 v68, v68, 0
	v_pk_max_i16 v69, v69, 0
	v_cvt_pk_bf16_f32 v96, v102, v103
	s_waitcnt lgkmcnt(2)
	v_mfma_f32_32x32x16_bf16 v[2:17], v[110:113], v[90:93], v[2:17]
	v_cvt_pk_bf16_f32 v97, v104, v105
	v_cvt_pk_bf16_f32 v74, v74, v75
	v_cvt_pk_bf16_f32 v75, v76, v77
	v_cvt_pk_bf16_f32 v76, v78, v79
	v_cvt_pk_bf16_f32 v77, v80, v81
	v_pk_max_i16 v94, v94, 0
	v_pk_max_i16 v95, v95, 0
	v_pk_max_i16 v96, v96, 0
	v_pk_max_i16 v97, v97, 0
	v_pk_max_i16 v74, v74, 0
	v_pk_max_i16 v75, v75, 0
	v_pk_max_i16 v76, v76, 0
	v_pk_max_i16 v77, v77, 0
	v_mfma_f32_32x32x16_bf16 v[18:33], v[110:113], v[66:69], v[18:33]
	s_waitcnt lgkmcnt(1)
	v_mfma_f32_32x32x16_bf16 v[34:49], v[98:101], v[66:69], v[34:49]
	ds_read_b128 v[66:69], v212 offset:22528
	v_mfma_f32_32x32x16_bf16 v[50:65], v[98:101], v[90:93], v[50:65]
	s_waitcnt lgkmcnt(1)
	v_mfma_f32_32x32x16_bf16 v[2:17], v[70:73], v[94:97], v[2:17]
	v_mfma_f32_32x32x16_bf16 v[18:33], v[70:73], v[74:77], v[18:33]
	ds_read_b128 v[78:81], v212 offset:3072
	s_waitcnt lgkmcnt(1)
	v_mfma_f32_32x32x16_bf16 v[50:65], v[66:69], v[94:97], v[50:65]
	ds_read_b128 v[90:93], v174 offset:33056
	ds_read_b128 v[94:97], v174 offset:33088
	ds_read_b128 v[98:101], v174 offset:33120
	ds_read_b128 v[70:73], v174 offset:33152
	v_mfma_f32_32x32x16_bf16 v[34:49], v[66:69], v[74:77], v[34:49]
	ds_read_b128 v[66:69], v212 offset:4096
	ds_read_b128 v[74:77], v212 offset:5120
	s_waitcnt lgkmcnt(3)
	v_mfma_f32_32x32x16_bf16 v[102:117], v[78:81], v[126:129], v[86:101]
	v_mfma_f32_32x32x16_bf16 v[86:101], v[78:81], v[134:137], v[86:101]
	s_waitcnt lgkmcnt(1)
	v_mfma_f32_32x32x16_bf16 v[86:101], v[66:69], v[146:149], v[86:101]
	v_mfma_f32_32x32x16_bf16 v[102:117], v[66:69], v[122:125], v[102:117]
	ds_read_b128 v[66:69], v212 offset:6144
	s_waitcnt lgkmcnt(1)
	v_mfma_f32_32x32x16_bf16 v[86:101], v[74:77], v[142:145], v[86:101]
	v_mfma_f32_32x32x16_bf16 v[102:117], v[74:77], v[130:133], v[102:117]
	ds_read_b128 v[74:77], v212 offset:15360
	s_waitcnt lgkmcnt(1)
	v_mfma_f32_32x32x16_bf16 v[86:101], v[66:69], v[138:141], v[86:101]
	v_mfma_f32_32x32x16_bf16 v[102:117], v[66:69], v[118:121], v[102:117]
	s_nop 10
	v_cvt_pk_bf16_f32 v78, v86, v87
	v_cvt_pk_bf16_f32 v80, v90, v91
	v_cvt_pk_bf16_f32 v79, v88, v89
	v_cvt_pk_bf16_f32 v81, v92, v93
	ds_read_b128 v[86:89], v212 offset:16384
	ds_read_b128 v[90:93], v212 offset:23552
	v_cvt_pk_bf16_f32 v66, v102, v103
	v_cvt_pk_bf16_f32 v67, v104, v105
	v_cvt_pk_bf16_f32 v68, v106, v107
	v_cvt_pk_bf16_f32 v69, v108, v109
	v_pk_max_i16 v66, v66, 0
	v_pk_max_i16 v67, v67, 0
	v_pk_max_i16 v68, v68, 0
	v_pk_max_i16 v69, v69, 0
	v_pk_max_i16 v78, v78, 0
	v_pk_max_i16 v79, v79, 0
	v_pk_max_i16 v80, v80, 0
	v_pk_max_i16 v81, v81, 0
	v_cvt_pk_bf16_f32 v94, v94, v95
	s_waitcnt lgkmcnt(2)
	v_mfma_f32_32x32x16_bf16 v[18:33], v[74:77], v[78:81], v[18:33]
	v_cvt_pk_bf16_f32 v95, v96, v97
	v_cvt_pk_bf16_f32 v96, v98, v99
	v_cvt_pk_bf16_f32 v97, v100, v101
	v_pk_max_i16 v94, v94, 0
	v_pk_max_i16 v95, v95, 0
	v_pk_max_i16 v96, v96, 0
	v_pk_max_i16 v97, v97, 0
	v_mfma_f32_32x32x16_bf16 v[2:17], v[74:77], v[66:69], v[2:17]
	v_cvt_pk_bf16_f32 v74, v110, v111
	v_cvt_pk_bf16_f32 v75, v112, v113
	v_cvt_pk_bf16_f32 v76, v114, v115
	v_cvt_pk_bf16_f32 v77, v116, v117
	v_pk_max_i16 v74, v74, 0
	v_pk_max_i16 v75, v75, 0
	v_pk_max_i16 v76, v76, 0
	v_pk_max_i16 v77, v77, 0
	s_waitcnt lgkmcnt(0)
	v_mfma_f32_32x32x16_bf16 v[50:65], v[90:93], v[66:69], v[50:65]
	ds_read_b128 v[66:69], v212 offset:24576
	v_mfma_f32_32x32x16_bf16 v[34:49], v[90:93], v[78:81], v[34:49]
	ds_read_b128 v[102:105], v212 offset:7168
	v_mfma_f32_32x32x16_bf16 v[2:17], v[86:89], v[74:77], v[2:17]
	s_waitcnt lgkmcnt(1)
	v_mfma_f32_32x32x16_bf16 v[50:65], v[66:69], v[74:77], v[50:65]
	ds_read_b128 v[74:77], v174 offset:33184
	ds_read_b128 v[78:81], v174 offset:33216
	v_mfma_f32_32x32x16_bf16 v[34:49], v[66:69], v[94:97], v[34:49]
	ds_read_b128 v[66:69], v212 offset:8192
	v_mfma_f32_32x32x16_bf16 v[18:33], v[86:89], v[94:97], v[18:33]
	s_waitcnt lgkmcnt(1)
	v_mfma_f32_32x32x16_bf16 v[86:101], v[102:105], v[126:129], v[70:85]
	v_mfma_f32_32x32x16_bf16 v[70:85], v[102:105], v[134:137], v[70:85]
	ds_read_b128 v[102:105], v212 offset:9216
	v_lshlrev_b32_e32 v135, 2, v1
	v_add_u32_e32 v134, v172, v174
	s_waitcnt lgkmcnt(1)
	v_mfma_f32_32x32x16_bf16 v[86:101], v[66:69], v[122:125], v[86:101]
	v_mfma_f32_32x32x16_bf16 v[70:85], v[66:69], v[146:149], v[70:85]
	ds_read_b128 v[66:69], v212 offset:10240
	s_waitcnt lgkmcnt(1)
	v_mfma_f32_32x32x16_bf16 v[86:101], v[102:105], v[130:133], v[86:101]
	v_mfma_f32_32x32x16_bf16 v[70:85], v[102:105], v[142:145], v[70:85]
	ds_read_b128 v[102:105], v212 offset:17408
	s_waitcnt lgkmcnt(1)
	v_mfma_f32_32x32x16_bf16 v[86:101], v[66:69], v[118:121], v[86:101]
	v_mfma_f32_32x32x16_bf16 v[70:85], v[66:69], v[138:141], v[70:85]
	s_nop 10
	v_cvt_pk_bf16_f32 v68, v90, v91
	v_cvt_pk_bf16_f32 v69, v92, v93
	ds_read_b128 v[90:93], v212 offset:25600
	v_cvt_pk_bf16_f32 v66, v86, v87
	v_cvt_pk_bf16_f32 v67, v88, v89
	v_pk_max_i16 v66, v66, 0
	v_pk_max_i16 v67, v67, 0
	v_pk_max_i16 v68, v68, 0
	v_pk_max_i16 v69, v69, 0
	v_cvt_pk_bf16_f32 v70, v70, v71
	v_cvt_pk_bf16_f32 v71, v72, v73
	s_waitcnt lgkmcnt(1)
	v_mfma_f32_32x32x16_bf16 v[2:17], v[102:105], v[66:69], v[2:17]
	v_cvt_pk_bf16_f32 v72, v74, v75
	v_cvt_pk_bf16_f32 v73, v76, v77
	ds_read_b128 v[74:77], v212 offset:18432
	v_cvt_pk_bf16_f32 v86, v94, v95
	v_cvt_pk_bf16_f32 v87, v96, v97
	v_cvt_pk_bf16_f32 v88, v98, v99
	s_waitcnt lgkmcnt(1)
	v_mfma_f32_32x32x16_bf16 v[50:65], v[90:93], v[66:69], v[50:65]
	ds_read_b128 v[66:69], v212 offset:26624
	v_cvt_pk_bf16_f32 v89, v100, v101
	v_pk_max_i16 v86, v86, 0
	v_pk_max_i16 v87, v87, 0
	v_pk_max_i16 v88, v88, 0
	v_pk_max_i16 v89, v89, 0
	v_pk_max_i16 v70, v70, 0
	v_pk_max_i16 v71, v71, 0
	v_pk_max_i16 v72, v72, 0
	v_pk_max_i16 v73, v73, 0
	v_cvt_pk_bf16_f32 v78, v78, v79
	v_cvt_pk_bf16_f32 v79, v80, v81
	s_waitcnt lgkmcnt(1)
	v_mfma_f32_32x32x16_bf16 v[2:17], v[74:77], v[86:89], v[2:17]
	v_cvt_pk_bf16_f32 v80, v82, v83
	v_cvt_pk_bf16_f32 v81, v84, v85
	v_pk_max_i16 v78, v78, 0
	v_pk_max_i16 v79, v79, 0
	v_pk_max_i16 v80, v80, 0
	v_pk_max_i16 v81, v81, 0
	s_waitcnt lgkmcnt(0)
	v_mfma_f32_32x32x16_bf16 v[50:65], v[66:69], v[86:89], v[50:65]
	v_mfma_f32_32x32x16_bf16 v[34:49], v[90:93], v[70:73], v[34:49]
	s_nop 10
	v_add_f32_e32 v130, v10, v58
	v_add_f32_e32 v131, v11, v59
	v_add_f32_e32 v132, v12, v60
	v_add_f32_e32 v133, v13, v61
	v_add_f32_e32 v138, v4, v52
	v_add_f32_e32 v139, v5, v53
	v_pk_add_f32 v[140:141], v[16:17], v[64:65]
	v_pk_add_f32 v[142:143], v[8:9], v[56:57]
	v_pk_add_f32 v[144:145], v[14:15], v[62:63]
	v_pk_add_f32 v[146:147], v[6:7], v[54:55]
	v_mfma_f32_32x32x16_bf16 v[18:33], v[102:105], v[70:73], v[18:33]
	ds_read2st64_b32 v[70:71], v135 offset0:133 offset1:134
	v_add_f32_e32 v148, v2, v50
	v_add_f32_e32 v149, v3, v51
	v_add_f32_e32 v144, v146, v144
	v_add_f32_e32 v145, v147, v145
	v_pk_add_f32 v[140:141], v[142:143], v[140:141]
	v_pk_add_f32 v[132:133], v[138:139], v[132:133]
	v_pk_add_f32 v[130:131], v[148:149], v[130:131]
	v_pk_add_f32 v[132:133], v[132:133], v[140:141]
	v_pk_add_f32 v[130:131], v[130:131], v[144:145]
	v_mfma_f32_32x32x16_bf16 v[34:49], v[66:69], v[78:81], v[34:49]
	s_waitcnt vmcnt(0) lgkmcnt(0)
	v_mul_f32_e32 v66, v175, v70
	v_add_f32_e32 v130, v131, v130
	v_add_f32_e32 v131, v132, v133
	ds_write_b32 v173, v66 offset:512
	v_mul_f32_e32 v66, v175, v71
	v_add_f32_e32 v130, v130, v131
	s_waitcnt lgkmcnt(0)
	ds_read_b128 v[102:105], v174 offset:34560
	ds_read_b128 v[98:101], v174 offset:34592
	ds_read_b128 v[110:113], v174 offset:34624
	ds_read_b128 v[106:109], v174 offset:34656
	ds_read_b128 v[114:117], v174 offset:34688
	ds_read_b128 v[122:125], v174 offset:34720
	ds_read_b128 v[118:121], v174 offset:34752
	ds_read_b128 v[126:129], v174 offset:34784
	v_mov_b32_dpp v66, v66 quad_perm:[1,0,3,2] row_mask:0xf bank_mask:0xf bound_ctrl:1
	v_mov_b32_e32 v131, v130
	v_fmac_f32_e32 v66, v175, v71
	s_nop 0
	v_permlane32_swap_b32_e32 v130, v131
	v_add_f32_dpp v66, v66, v66 quad_perm:[2,3,0,1] row_mask:0xf bank_mask:0xf bound_ctrl:1
	v_add_f32_e32 v130, v130, v131
	v_fmamk_f32 v65, v130, 0xbc800000, v65
	v_add_f32_dpp v66, v66, v66 row_half_mirror row_mask:0xf bank_mask:0xf bound_ctrl:1
	v_fmamk_f32 v64, v130, 0xbc800000, v64
	v_fmamk_f32 v63, v130, 0xbc800000, v63
	v_fmamk_f32 v62, v130, 0xbc800000, v62
	v_fmamk_f32 v61, v130, 0xbc800000, v61
	v_fmamk_f32 v60, v130, 0xbc800000, v60
	v_fmamk_f32 v59, v130, 0xbc800000, v59
	v_fmamk_f32 v58, v130, 0xbc800000, v58
	v_fmamk_f32 v57, v130, 0xbc800000, v57
	v_fmamk_f32 v56, v130, 0xbc800000, v56
	v_fmamk_f32 v55, v130, 0xbc800000, v55
	v_fmamk_f32 v54, v130, 0xbc800000, v54
	v_fmamk_f32 v53, v130, 0xbc800000, v53
	v_fmamk_f32 v52, v130, 0xbc800000, v52
	v_fmamk_f32 v51, v130, 0xbc800000, v51
	v_fmac_f32_e32 v50, 0xbc800000, v130
	v_add_f32_dpp v66, v66, v66 row_ror:8 row_mask:0xf bank_mask:0xf bound_ctrl:1
	v_fmamk_f32 v17, v130, 0xbc800000, v17
	v_fmamk_f32 v16, v130, 0xbc800000, v16
	v_fmamk_f32 v15, v130, 0xbc800000, v15
	v_fmamk_f32 v14, v130, 0xbc800000, v14
	v_fmamk_f32 v13, v130, 0xbc800000, v13
	v_fmamk_f32 v12, v130, 0xbc800000, v12
	v_fmamk_f32 v11, v130, 0xbc800000, v11
	v_fmamk_f32 v10, v130, 0xbc800000, v10
	v_fmamk_f32 v9, v130, 0xbc800000, v9
	v_fmamk_f32 v8, v130, 0xbc800000, v8
	v_fmamk_f32 v7, v130, 0xbc800000, v7
	v_fmamk_f32 v6, v130, 0xbc800000, v6
	v_fmamk_f32 v5, v130, 0xbc800000, v5
	v_fmamk_f32 v4, v130, 0xbc800000, v4
	v_fmamk_f32 v3, v130, 0xbc800000, v3
	v_fmac_f32_e32 v2, 0xbc800000, v130
	v_pk_mul_f32 v[130:131], v[54:55], v[54:55]
	v_pk_mul_f32 v[132:133], v[62:63], v[62:63]
	v_pk_mul_f32 v[138:139], v[50:51], v[50:51]
	v_pk_mul_f32 v[140:141], v[58:59], v[58:59]
	v_pk_mul_f32 v[142:143], v[56:57], v[56:57]
	v_pk_mul_f32 v[144:145], v[64:65], v[64:65]
	v_pk_mul_f32 v[146:147], v[52:53], v[52:53]
	v_pk_mul_f32 v[148:149], v[60:61], v[60:61]
	v_mov_b32_e32 v67, v66
	v_pk_fma_f32 v[148:149], v[12:13], v[12:13], v[148:149]
	v_pk_fma_f32 v[146:147], v[4:5], v[4:5], v[146:147]
	v_pk_fma_f32 v[144:145], v[16:17], v[16:17], v[144:145]
	v_pk_fma_f32 v[142:143], v[8:9], v[8:9], v[142:143]
	v_pk_fma_f32 v[140:141], v[10:11], v[10:11], v[140:141]
	v_pk_fma_f32 v[138:139], v[2:3], v[2:3], v[138:139]
	v_pk_fma_f32 v[132:133], v[14:15], v[14:15], v[132:133]
	v_pk_fma_f32 v[130:131], v[6:7], v[6:7], v[130:131]
	v_permlane16_swap_b32_e32 v66, v67
	v_pk_add_f32 v[130:131], v[130:131], v[132:133]
	v_pk_add_f32 v[132:133], v[138:139], v[140:141]
	v_pk_add_f32 v[138:139], v[142:143], v[144:145]
	v_pk_add_f32 v[140:141], v[146:147], v[148:149]
	v_mfma_f32_32x32x16_bf16 v[18:33], v[74:77], v[78:81], v[18:33]
	v_add_f32_e32 v136, v66, v67
	ds_read_b128 v[70:73], v134 offset:512
	ds_read_b128 v[66:69], v134 offset:544
	ds_read_b128 v[78:81], v134 offset:576
	ds_read_b128 v[74:77], v134 offset:608
	ds_read_b128 v[82:85], v134 offset:640
	ds_read_b128 v[90:93], v134 offset:672
	ds_read_b128 v[86:89], v134 offset:704
	ds_read_b128 v[94:97], v134 offset:736
	v_pk_add_f32 v[138:139], v[140:141], v[138:139]
	v_pk_add_f32 v[130:131], v[132:133], v[130:131]
	s_waitcnt lgkmcnt(8)
	v_pk_mul_f32 v[140:141], v[126:127], v[62:63]
	v_pk_mov_b32 v[132:133], v[130:131], v[138:139] op_sel:[1,0]
	v_mov_b32_e32 v131, v139
	v_pk_mul_f32 v[138:139], v[122:123], v[54:55]
	v_pk_mul_f32 v[142:143], v[114:115], v[50:51]
	v_pk_mul_f32 v[144:145], v[118:119], v[58:59]
	v_pk_mul_f32 v[146:147], v[124:125], v[56:57]
	v_pk_mul_f32 v[148:149], v[128:129], v[64:65]
	v_pk_mul_f32 v[154:155], v[116:117], v[52:53]
	v_pk_mul_f32 v[156:157], v[120:121], v[60:61]
	v_pk_fma_f32 v[154:155], v[104:105], v[4:5], v[154:155]
	v_pk_fma_f32 v[156:157], v[112:113], v[12:13], v[156:157]
	v_pk_fma_f32 v[148:149], v[108:109], v[16:17], v[148:149]
	v_pk_fma_f32 v[146:147], v[100:101], v[8:9], v[146:147]
	v_pk_fma_f32 v[144:145], v[110:111], v[10:11], v[144:145]
	v_pk_fma_f32 v[142:143], v[102:103], v[2:3], v[142:143]
	v_pk_fma_f32 v[140:141], v[106:107], v[14:15], v[140:141]
	v_pk_fma_f32 v[138:139], v[98:99], v[6:7], v[138:139]
	v_pk_add_f32 v[130:131], v[132:133], v[130:131]
	v_pk_add_f32 v[138:139], v[138:139], v[140:141]
	v_pk_add_f32 v[140:141], v[142:143], v[144:145]
	v_pk_add_f32 v[142:143], v[146:147], v[148:149]
	v_pk_add_f32 v[144:145], v[154:155], v[156:157]
	v_pk_add_f32 v[132:133], v[130:131], v[130:131] op_sel:[0,1] op_sel_hi:[1,0]
	v_pk_add_f32 v[142:143], v[144:145], v[142:143]
	v_pk_add_f32 v[138:139], v[140:141], v[138:139]
	v_add_f32_e32 v133, v142, v143
	v_add_f32_e32 v130, v138, v139
	s_waitcnt lgkmcnt(2)
	v_pk_mul_f32 v[138:139], v[90:91], v[54:55]
	s_waitcnt lgkmcnt(0)
	v_pk_mul_f32 v[140:141], v[94:95], v[62:63]
	v_pk_mul_f32 v[142:143], v[82:83], v[50:51]
	v_pk_mul_f32 v[144:145], v[86:87], v[58:59]
	v_pk_mul_f32 v[146:147], v[92:93], v[56:57]
	v_pk_mul_f32 v[148:149], v[96:97], v[64:65]
	v_pk_mul_f32 v[154:155], v[84:85], v[52:53]
	v_pk_mul_f32 v[156:157], v[88:89], v[60:61]
	v_add_f32_e32 v130, v130, v133
	v_pk_fma_f32 v[156:157], v[80:81], v[12:13], v[156:157]
	v_pk_fma_f32 v[154:155], v[72:73], v[4:5], v[154:155]
	v_pk_fma_f32 v[148:149], v[76:77], v[16:17], v[148:149]
	v_pk_fma_f32 v[146:147], v[68:69], v[8:9], v[146:147]
	v_pk_fma_f32 v[144:145], v[78:79], v[10:11], v[144:145]
	v_pk_fma_f32 v[142:143], v[70:71], v[2:3], v[142:143]
	v_pk_fma_f32 v[140:141], v[74:75], v[14:15], v[140:141]
	v_pk_fma_f32 v[138:139], v[66:67], v[6:7], v[138:139]
	v_mov_b32_e32 v133, v130
	v_pk_add_f32 v[138:139], v[138:139], v[140:141]
	v_pk_add_f32 v[140:141], v[142:143], v[144:145]
	v_pk_add_f32 v[142:143], v[146:147], v[148:149]
	v_pk_add_f32 v[144:145], v[154:155], v[156:157]
	v_permlane32_swap_b32_e32 v130, v133
	v_pk_add_f32 v[142:143], v[144:145], v[142:143]
	v_add_f32_e32 v160, v130, v133
	v_pk_add_f32 v[138:139], v[140:141], v[138:139]
	v_add_f32_e32 v133, v142, v143
	v_pk_add_f32 v[140:141], v[26:27], v[42:43]
	v_pk_add_f32 v[142:143], v[28:29], v[44:45]
	v_pk_add_f32 v[144:145], v[20:21], v[36:37]
	v_pk_add_f32 v[146:147], v[32:33], v[48:49]
	v_pk_add_f32 v[148:149], v[24:25], v[40:41]
	v_pk_add_f32 v[154:155], v[30:31], v[46:47]
	v_pk_add_f32 v[156:157], v[22:23], v[38:39]
	v_pk_add_f32 v[158:159], v[18:19], v[34:35]
	v_pk_add_f32 v[154:155], v[156:157], v[154:155]
	v_pk_add_f32 v[146:147], v[148:149], v[146:147]
	v_pk_add_f32 v[142:143], v[144:145], v[142:143]
	v_pk_add_f32 v[140:141], v[158:159], v[140:141]
	v_pk_add_f32 v[142:143], v[142:143], v[146:147]
	v_pk_add_f32 v[140:141], v[140:141], v[154:155]
	v_add_f32_e32 v130, v138, v139
	v_add_f32_e32 v140, v141, v140
	v_add_f32_e32 v141, v142, v143
	v_add_f32_e32 v133, v130, v133
	v_add_f32_e32 v140, v140, v141
	v_mov_b32_e32 v131, v132
	v_mov_b32_e32 v130, v140
	s_nop 1
	v_permlane32_swap_b32_e32 v140, v130
	v_add_f32_e32 v130, v140, v130
	v_fmamk_f32 v49, v130, 0xbc800000, v49
	v_fmamk_f32 v48, v130, 0xbc800000, v48
	v_fmamk_f32 v47, v130, 0xbc800000, v47
	v_fmamk_f32 v46, v130, 0xbc800000, v46
	v_fmamk_f32 v45, v130, 0xbc800000, v45
	v_fmamk_f32 v44, v130, 0xbc800000, v44
	v_fmamk_f32 v43, v130, 0xbc800000, v43
	v_fmamk_f32 v42, v130, 0xbc800000, v42
	v_fmamk_f32 v41, v130, 0xbc800000, v41
	v_fmamk_f32 v40, v130, 0xbc800000, v40
	v_fmamk_f32 v39, v130, 0xbc800000, v39
	v_fmamk_f32 v38, v130, 0xbc800000, v38
	v_fmamk_f32 v37, v130, 0xbc800000, v37
	v_fmamk_f32 v36, v130, 0xbc800000, v36
	v_fmamk_f32 v35, v130, 0xbc800000, v35
	v_fmac_f32_e32 v34, 0xbc800000, v130
	v_fmamk_f32 v33, v130, 0xbc800000, v33
	v_fmamk_f32 v32, v130, 0xbc800000, v32
	v_fmamk_f32 v31, v130, 0xbc800000, v31
	v_fmamk_f32 v30, v130, 0xbc800000, v30
	v_fmamk_f32 v29, v130, 0xbc800000, v29
	v_fmamk_f32 v28, v130, 0xbc800000, v28
	v_fmamk_f32 v27, v130, 0xbc800000, v27
	v_fmamk_f32 v26, v130, 0xbc800000, v26
	v_fmamk_f32 v25, v130, 0xbc800000, v25
	v_fmamk_f32 v24, v130, 0xbc800000, v24
	v_fmamk_f32 v23, v130, 0xbc800000, v23
	v_fmamk_f32 v22, v130, 0xbc800000, v22
	v_fmamk_f32 v21, v130, 0xbc800000, v21
	v_fmamk_f32 v20, v130, 0xbc800000, v20
	v_fmamk_f32 v19, v130, 0xbc800000, v19
	v_fmac_f32_e32 v18, 0xbc800000, v130
	v_pk_mul_f32 v[140:141], v[38:39], v[38:39]
	v_pk_mul_f32 v[142:143], v[46:47], v[46:47]
	v_pk_mul_f32 v[144:145], v[34:35], v[34:35]
	v_pk_mul_f32 v[146:147], v[42:43], v[42:43]
	v_pk_mul_f32 v[148:149], v[40:41], v[40:41]
	v_pk_mul_f32 v[154:155], v[48:49], v[48:49]
	v_pk_mul_f32 v[156:157], v[36:37], v[36:37]
	v_pk_mul_f32 v[158:159], v[44:45], v[44:45]
	v_pk_fma_f32 v[156:157], v[20:21], v[20:21], v[156:157]
	v_pk_fma_f32 v[158:159], v[28:29], v[28:29], v[158:159]
	v_pk_fma_f32 v[154:155], v[32:33], v[32:33], v[154:155]
	v_pk_fma_f32 v[148:149], v[24:25], v[24:25], v[148:149]
	v_pk_fma_f32 v[146:147], v[26:27], v[26:27], v[146:147]
	v_pk_fma_f32 v[144:145], v[18:19], v[18:19], v[144:145]
	v_pk_fma_f32 v[142:143], v[30:31], v[30:31], v[142:143]
	v_pk_fma_f32 v[140:141], v[22:23], v[22:23], v[140:141]
	v_permlane32_swap_b32_e32 v132, v131
	v_pk_add_f32 v[140:141], v[140:141], v[142:143]
	v_pk_add_f32 v[142:143], v[144:145], v[146:147]
	v_pk_add_f32 v[144:145], v[148:149], v[154:155]
	v_pk_add_f32 v[146:147], v[156:157], v[158:159]
	v_pk_add_f32 v[140:141], v[142:143], v[140:141]
	v_pk_add_f32 v[144:145], v[146:147], v[144:145]
	v_pk_mul_f32 v[122:123], v[122:123], v[38:39]
	v_pk_mov_b32 v[142:143], v[140:141], v[144:145] op_sel:[1,0]
	v_mov_b32_e32 v141, v145
	v_pk_add_f32 v[140:141], v[142:143], v[140:141]
	v_pk_mul_f32 v[126:127], v[126:127], v[46:47]
	v_pk_add_f32 v[140:141], v[140:141], v[140:141] op_sel:[0,1] op_sel_hi:[1,0]
	v_pk_mul_f32 v[114:115], v[114:115], v[34:35]
	v_mov_b32_e32 v130, v140
	s_nop 1
	v_permlane32_swap_b32_e32 v140, v130
	v_mov_b32_e32 v141, v132
	v_pk_add_f32 v[130:131], v[140:141], v[130:131]
	v_pk_mul_f32 v[118:119], v[118:119], v[42:43]
	v_pk_fma_f32 v[130:131], v[130:131], s[0:1], v[152:153] op_sel_hi:[1,0,0]
	v_pk_mul_f32 v[124:125], v[124:125], v[40:41]
	v_pk_mul_f32 v[128:129], v[128:129], v[48:49]
	v_pk_mul_f32 v[116:117], v[116:117], v[36:37]
	v_pk_mul_f32 v[120:121], v[120:121], v[44:45]
	v_pk_fma_f32 v[112:113], v[112:113], v[28:29], v[120:121]
	v_pk_fma_f32 v[104:105], v[104:105], v[20:21], v[116:117]
	v_pk_fma_f32 v[108:109], v[108:109], v[32:33], v[128:129]
	v_pk_fma_f32 v[100:101], v[100:101], v[24:25], v[124:125]
	v_pk_fma_f32 v[110:111], v[110:111], v[26:27], v[118:119]
	v_pk_fma_f32 v[102:103], v[102:103], v[18:19], v[114:115]
	v_pk_fma_f32 v[106:107], v[106:107], v[30:31], v[126:127]
	v_pk_fma_f32 v[98:99], v[98:99], v[22:23], v[122:123]
	v_rsq_f32_e32 v131, v131
	v_pk_add_f32 v[98:99], v[98:99], v[106:107]
	v_pk_add_f32 v[102:103], v[102:103], v[110:111]
	v_pk_add_f32 v[100:101], v[100:101], v[108:109]
	v_pk_add_f32 v[104:105], v[104:105], v[112:113]
	v_rsq_f32_e32 v132, v130
	v_pk_add_f32 v[100:101], v[104:105], v[100:101]
	v_pk_add_f32 v[98:99], v[102:103], v[98:99]
	v_add_f32_e32 v98, v98, v99
	v_add_f32_e32 v99, v100, v101
	v_add_f32_e32 v98, v98, v99
	v_mov_b32_e32 v99, v98
	v_pk_mul_f32 v[90:91], v[90:91], v[38:39]
	v_pk_mul_f32 v[94:95], v[94:95], v[46:47]
	v_pk_mul_f32 v[82:83], v[82:83], v[34:35]
	v_pk_mul_f32 v[86:87], v[86:87], v[42:43]
	v_permlane32_swap_b32_e32 v98, v99
	v_pk_fma_f32 v[78:79], v[78:79], v[26:27], v[86:87]
	v_pk_fma_f32 v[70:71], v[70:71], v[18:19], v[82:83]
	v_pk_fma_f32 v[74:75], v[74:75], v[30:31], v[94:95]
	v_pk_fma_f32 v[66:67], v[66:67], v[22:23], v[90:91]
	v_mov_b32_e32 v130, v131
	v_mov_b32_e32 v131, v132
	v_add_f32_e32 v98, v98, v99
	v_pk_add_f32 v[66:67], v[66:67], v[74:75]
	v_pk_add_f32 v[70:71], v[70:71], v[78:79]
	v_mul_f32_e32 v139, v160, v130
	v_mul_f32_e32 v98, v98, v131
	v_pk_add_f32 v[66:67], v[70:71], v[66:67]
	v_cmp_gt_u32_e32 vcc, 32, v1
	v_add_f32_e32 v66, v66, v67
	v_pk_mul_f32 v[92:93], v[92:93], v[40:41]
	v_cndmask_b32_e32 v67, v98, v139, vcc
	v_add_f32_e32 v67, s12, v67
	v_pk_mul_f32 v[96:97], v[96:97], v[48:49]
	v_pk_mul_f32 v[84:85], v[84:85], v[36:37]
	v_pk_mul_f32 v[88:89], v[88:89], v[44:45]
	v_mul_f32_e32 v67, 0xbfb8aa3b, v67
	v_pk_fma_f32 v[80:81], v[80:81], v[28:29], v[88:89]
	v_pk_fma_f32 v[72:73], v[72:73], v[20:21], v[84:85]
	v_pk_fma_f32 v[76:77], v[76:77], v[32:33], v[96:97]
	v_pk_fma_f32 v[68:69], v[68:69], v[24:25], v[92:93]
	v_exp_f32_e32 v70, v67
	v_pk_add_f32 v[68:69], v[68:69], v[76:77]
	v_pk_add_f32 v[72:73], v[72:73], v[80:81]
	v_cmp_lt_i32_e64 s[0:1], 0, v151
	v_pk_add_f32 v[68:69], v[72:73], v[68:69]
	v_mov_b32_e32 v137, v136
	v_add_f32_e32 v67, v68, v69
	v_add_f32_e32 v67, v66, v67
	v_add_f32_e32 v66, 1.0, v70
	v_rcp_f32_e32 v66, v66
	v_mov_b32_e32 v69, 0xff800000
	v_mov_b32_e32 v138, v133
	v_mov_b32_e32 v68, v67
	v_cndmask_b32_e64 v70, v69, v66, s[0:1]
	v_mbcnt_lo_u32_b32 v66, -1, 0
	v_mbcnt_hi_u32_b32 v66, -1, v66
	v_permlane32_swap_b32_e32 v136, v137
	v_permlane32_swap_b32_e32 v133, v138
	v_permlane32_swap_b32_e32 v67, v68
	v_and_b32_e32 v86, 64, v66
	s_mov_b32 s14, 8
	s_mov_b32 s13, 0
	v_mov_b32_e32 v66, 0
	s_waitcnt lgkmcnt(0)
	.p2align 6
